# grid barrier: L1/L2 invalidate issued at arrival (overlaps the spin) instead of after the release; plus batched tail-partial loads in MoE combine
# speedup vs baseline: 1.0133x; 1.0070x over previous
; __device__ __forceinline__ unsigned xb_ld(unsigned* p)              { return __hip_atomic_load(p, __ATOMIC_RELAXED, __HIP_MEMORY_SCOPE_AGENT); }
; __device__ __forceinline__ unsigned xb_add(unsigned* p, unsigned v) { return __hip_atomic_fetch_add(p, v, __ATOMIC_RELAXED, __HIP_MEMORY_SCOPE_AGENT); }
; #define XB_SPIN(cond, bar) do { unsigned _sp = 0; while (cond) { __builtin_amdgcn_s_sleep(1); \
;     if ((++_sp & 255u) == 0u) { if (xb_ld(&(bar)[XB_TMO])) break; if (_sp > XB_SPIN_CAP) { atomicAdd(&(bar)[XB_TMO], 1u); break; } } } } while (0)
; __device__ __forceinline__ void xcd_barrier(const XcdBarrier& b) {
;     ...
;         unsigned nloc = b.st[0], nx = b.st[1];
;         if (nloc == 0u) { xcd_barrier_complete(bar, b.x, nloc, nx); b.st[0] = nloc; b.st[1] = nx; }
;         const unsigned old = xb_add(&bar[XB_XSUB(b.x)], 1u);
;         const unsigned gen = old / nloc;
;         if (old + 1u == (gen + 1u) * nloc) {
;             __builtin_amdgcn_fence(__ATOMIC_RELEASE, "agent");
;             asm volatile("s_waitcnt vmcnt(0)" ::: "memory");
;             const unsigned og = xb_add(&bar[XB_TOP], 1u);
;             const unsigned tg = og / nx;
;             if (og + 1u == (tg + 1u) * nx) xb_add(&bar[XB_TOPGEN], 1u);
;             else XB_SPIN(xb_ld(&bar[XB_TOPGEN]) == tg, bar);
;             __builtin_amdgcn_fence(__ATOMIC_ACQUIRE, "agent");
;             xb_add(&bar[XB_XGEN(b.x)], 1u);
;             asm volatile("s_waitcnt vmcnt(0)" ::: "memory");
;         } else {
;             XB_SPIN(xb_ld(&bar[XB_XGEN(b.x)]) == gen, bar);
.LBB0_120:
	s_or_b64 exec, exec, s[18:19]
	v_cvt_f32_u32_e32 v5, v3
	s_waitcnt vmcnt(0)
	v_readfirstlane_b32 s16, v4
	v_sub_u32_e32 v4, 0, v3
	v_rcp_iflag_f32_e32 v5, v5
	v_add_u32_e32 v6, s16, v0
	v_mul_f32_e32 v5, 0x4f7ffffe, v5
	v_cvt_u32_f32_e32 v5, v5
	v_mul_lo_u32 v0, v4, v5
	v_mul_hi_u32 v0, v5, v0
	v_add_u32_e32 v0, v5, v0
	v_mul_hi_u32 v0, v6, v0
	v_mul_lo_u32 v4, v0, v3
	v_sub_u32_e32 v4, v6, v4
	v_add_u32_e32 v5, 1, v0
	v_cmp_ge_u32_e32 vcc, v4, v3
	s_nop 1
	v_cndmask_b32_e32 v0, v0, v5, vcc
	v_sub_u32_e32 v5, v4, v3
	v_cndmask_b32_e32 v4, v4, v5, vcc
	v_add_u32_e32 v5, 1, v0
	v_cmp_ge_u32_e32 vcc, v4, v3
	v_add_u32_e32 v4, 1, v6
	s_nop 0
	v_cndmask_b32_e32 v0, v0, v5, vcc
	v_mul_lo_u32 v5, v3, v0
	v_add_u32_e32 v3, v5, v3
	v_cmp_ne_u32_e32 vcc, v4, v3
	s_and_saveexec_b64 s[16:17], vcc
	s_xor_b64 s[16:17], exec, s[16:17]
	s_cbranch_execz .LBB0_134
	s_waitcnt lgkmcnt(0)
	buffer_inv sc1
	v_mov_b32_e32 v2, 0x2000
	global_load_dword v2, v2, s[14:15] offset:1024 sc1
	s_add_u32 s18, s14, 0x2400
	s_addc_u32 s19, s15, 0
	s_waitcnt vmcnt(0)
	v_cmp_eq_u32_e32 vcc, v2, v0
	s_and_saveexec_b64 s[20:21], vcc
	s_cbranch_execz .LBB0_133
	s_mov_b32 s34, 1
	s_mov_b64 s[22:23], 0
	s_branch .LBB0_124

; __device__ __forceinline__ unsigned xb_ld(unsigned* p)              { return __hip_atomic_load(p, __ATOMIC_RELAXED, __HIP_MEMORY_SCOPE_AGENT); }
; __device__ __forceinline__ unsigned xb_add(unsigned* p, unsigned v) { return __hip_atomic_fetch_add(p, v, __ATOMIC_RELAXED, __HIP_MEMORY_SCOPE_AGENT); }
; #define XB_SPIN(cond, bar) do { unsigned _sp = 0; while (cond) { __builtin_amdgcn_s_sleep(1); \
;     if ((++_sp & 255u) == 0u) { if (xb_ld(&(bar)[XB_TMO])) break; if (_sp > XB_SPIN_CAP) { atomicAdd(&(bar)[XB_TMO], 1u); break; } } } } while (0)
; __device__ __forceinline__ void xcd_barrier(const XcdBarrier& b) {
;     ...
;         if (old + 1u == (gen + 1u) * nloc) {
;             __builtin_amdgcn_fence(__ATOMIC_RELEASE, "agent");
;             asm volatile("s_waitcnt vmcnt(0)" ::: "memory");
;             const unsigned og = xb_add(&bar[XB_TOP], 1u);
;             const unsigned tg = og / nx;
;             if (og + 1u == (tg + 1u) * nx) xb_add(&bar[XB_TOPGEN], 1u);
;             else XB_SPIN(xb_ld(&bar[XB_TOPGEN]) == tg, bar);
;             __builtin_amdgcn_fence(__ATOMIC_ACQUIRE, "agent");
;             xb_add(&bar[XB_XGEN(b.x)], 1u);
;             asm volatile("s_waitcnt vmcnt(0)" ::: "memory");
;         } else {
;             XB_SPIN(xb_ld(&bar[XB_XGEN(b.x)]) == gen, bar);
;             __builtin_amdgcn_fence(__ATOMIC_ACQUIRE, "agent");
.LBB0_133:
	s_or_b64 exec, exec, s[20:21]
	s_waitcnt vmcnt(0)
	s_waitcnt vmcnt(0)
.LBB0_134:
	s_andn2_saveexec_b64 s[16:17], s[16:17]
	s_cbranch_execz .LBB0_154
	s_mov_b64 s[16:17], exec
	buffer_wbl2 sc1
	s_waitcnt lgkmcnt(0)
	s_waitcnt vmcnt(0)
	buffer_inv sc1
	v_mbcnt_lo_u32_b32 v0, s16, 0
	v_mbcnt_hi_u32_b32 v0, s17, v0
	v_cmp_eq_u32_e32 vcc, 0, v0
	s_and_saveexec_b64 s[18:19], vcc
	s_cbranch_execz .LBB0_137
	s_bcnt1_i32_b64 s16, s[16:17]
	v_mov_b32_e32 v3, s16
	v_mov_b32_e32 v4, 0x3000
	global_atomic_add v3, v4, v3, s[12:13] offset:1024 sc0

; __device__ __forceinline__ unsigned xb_ld(unsigned* p)              { return __hip_atomic_load(p, __ATOMIC_RELAXED, __HIP_MEMORY_SCOPE_AGENT); }
; __device__ __forceinline__ unsigned xb_add(unsigned* p, unsigned v) { return __hip_atomic_fetch_add(p, v, __ATOMIC_RELAXED, __HIP_MEMORY_SCOPE_AGENT); }
; #define XB_SPIN(cond, bar) do { unsigned _sp = 0; while (cond) { __builtin_amdgcn_s_sleep(1); \
;     if ((++_sp & 255u) == 0u) { if (xb_ld(&(bar)[XB_TMO])) break; if (_sp > XB_SPIN_CAP) { atomicAdd(&(bar)[XB_TMO], 1u); break; } } } } while (0)
; __device__ __forceinline__ void xcd_barrier(const XcdBarrier& b) {
;     ...
;             const unsigned og = xb_add(&bar[XB_TOP], 1u);
;             const unsigned tg = og / nx;
;             if (og + 1u == (tg + 1u) * nx) xb_add(&bar[XB_TOPGEN], 1u);
;             else XB_SPIN(xb_ld(&bar[XB_TOPGEN]) == tg, bar);
;             __builtin_amdgcn_fence(__ATOMIC_ACQUIRE, "agent");
;             xb_add(&bar[XB_XGEN(b.x)], 1u);
.LBB0_151:
	s_or_b64 exec, exec, s[12:13]
	s_mov_b64 s[12:13], exec
	v_mbcnt_lo_u32_b32 v0, s12, 0
	v_mbcnt_hi_u32_b32 v0, s13, v0
	v_cmp_eq_u32_e32 vcc, 0, v0
	s_waitcnt vmcnt(0)
	s_and_saveexec_b64 s[16:17], vcc
	s_cbranch_execz .LBB0_153
	s_bcnt1_i32_b64 s12, s[12:13]
	v_mov_b32_e32 v0, s12
	v_mov_b32_e32 v2, 0x2000
	global_atomic_add v2, v0, s[14:15] offset:1024

; __device__ __forceinline__ unsigned xb_ld(unsigned* p)              { return __hip_atomic_load(p, __ATOMIC_RELAXED, __HIP_MEMORY_SCOPE_AGENT); }
; __device__ __forceinline__ unsigned xb_add(unsigned* p, unsigned v) { return __hip_atomic_fetch_add(p, v, __ATOMIC_RELAXED, __HIP_MEMORY_SCOPE_AGENT); }
; #define XB_SPIN(cond, bar) do { unsigned _sp = 0; while (cond) { __builtin_amdgcn_s_sleep(1); \
;     if ((++_sp & 255u) == 0u) { if (xb_ld(&(bar)[XB_TMO])) break; if (_sp > XB_SPIN_CAP) { atomicAdd(&(bar)[XB_TMO], 1u); break; } } } } while (0)
; __device__ __forceinline__ void xcd_barrier(const XcdBarrier& b) {
;     ...
;         unsigned nloc = b.st[0], nx = b.st[1];
;         if (nloc == 0u) { xcd_barrier_complete(bar, b.x, nloc, nx); b.st[0] = nloc; b.st[1] = nx; }
;         const unsigned old = xb_add(&bar[XB_XSUB(b.x)], 1u);
;         const unsigned gen = old / nloc;
;         if (old + 1u == (gen + 1u) * nloc) {
;             __builtin_amdgcn_fence(__ATOMIC_RELEASE, "agent");
;             asm volatile("s_waitcnt vmcnt(0)" ::: "memory");
;             const unsigned og = xb_add(&bar[XB_TOP], 1u);
;             const unsigned tg = og / nx;
;             if (og + 1u == (tg + 1u) * nx) xb_add(&bar[XB_TOPGEN], 1u);
;             else XB_SPIN(xb_ld(&bar[XB_TOPGEN]) == tg, bar);
;             __builtin_amdgcn_fence(__ATOMIC_ACQUIRE, "agent");
;             xb_add(&bar[XB_XGEN(b.x)], 1u);
;             asm volatile("s_waitcnt vmcnt(0)" ::: "memory");
;         } else {
;             XB_SPIN(xb_ld(&bar[XB_XGEN(b.x)]) == gen, bar);
.LBB0_389:
	s_or_b64 exec, exec, s[18:19]
	v_cvt_f32_u32_e32 v5, v3
	s_waitcnt vmcnt(0)
	v_readfirstlane_b32 s16, v4
	v_sub_u32_e32 v4, 0, v3
	v_rcp_iflag_f32_e32 v5, v5
	v_add_u32_e32 v6, s16, v0
	v_mul_f32_e32 v5, 0x4f7ffffe, v5
	v_cvt_u32_f32_e32 v5, v5
	v_mul_lo_u32 v0, v4, v5
	v_mul_hi_u32 v0, v5, v0
	v_add_u32_e32 v0, v5, v0
	v_mul_hi_u32 v0, v6, v0
	v_mul_lo_u32 v4, v0, v3
	v_sub_u32_e32 v4, v6, v4
	v_add_u32_e32 v5, 1, v0
	v_cmp_ge_u32_e32 vcc, v4, v3
	s_nop 1
	v_cndmask_b32_e32 v0, v0, v5, vcc
	v_sub_u32_e32 v5, v4, v3
	v_cndmask_b32_e32 v4, v4, v5, vcc
	v_add_u32_e32 v5, 1, v0
	v_cmp_ge_u32_e32 vcc, v4, v3
	v_add_u32_e32 v4, 1, v6
	s_nop 0
	v_cndmask_b32_e32 v0, v0, v5, vcc
	v_mul_lo_u32 v5, v3, v0
	v_add_u32_e32 v3, v5, v3
	v_cmp_ne_u32_e32 vcc, v4, v3
	s_and_saveexec_b64 s[16:17], vcc
	s_xor_b64 s[16:17], exec, s[16:17]
	s_cbranch_execz .LBB0_403
	s_waitcnt lgkmcnt(0)
	buffer_inv sc1
	v_mov_b32_e32 v2, 0x2000
	global_load_dword v2, v2, s[14:15] offset:1024 sc1
	s_add_u32 s18, s14, 0x2400
	s_addc_u32 s19, s15, 0
	s_waitcnt vmcnt(0)
	v_cmp_eq_u32_e32 vcc, v2, v0
	s_and_saveexec_b64 s[20:21], vcc
	s_cbranch_execz .LBB0_402
	s_mov_b32 s35, 1
	s_mov_b64 s[22:23], 0
	s_branch .LBB0_393

; __device__ __forceinline__ unsigned xb_ld(unsigned* p)              { return __hip_atomic_load(p, __ATOMIC_RELAXED, __HIP_MEMORY_SCOPE_AGENT); }
; __device__ __forceinline__ unsigned xb_add(unsigned* p, unsigned v) { return __hip_atomic_fetch_add(p, v, __ATOMIC_RELAXED, __HIP_MEMORY_SCOPE_AGENT); }
; #define XB_SPIN(cond, bar) do { unsigned _sp = 0; while (cond) { __builtin_amdgcn_s_sleep(1); \
;     if ((++_sp & 255u) == 0u) { if (xb_ld(&(bar)[XB_TMO])) break; if (_sp > XB_SPIN_CAP) { atomicAdd(&(bar)[XB_TMO], 1u); break; } } } } while (0)
; __device__ __forceinline__ void xcd_barrier(const XcdBarrier& b) {
;     ...
;         unsigned nloc = b.st[0], nx = b.st[1];
;         if (nloc == 0u) { xcd_barrier_complete(bar, b.x, nloc, nx); b.st[0] = nloc; b.st[1] = nx; }
;         const unsigned old = xb_add(&bar[XB_XSUB(b.x)], 1u);
;         const unsigned gen = old / nloc;
;         if (old + 1u == (gen + 1u) * nloc) {
;             __builtin_amdgcn_fence(__ATOMIC_RELEASE, "agent");
;             asm volatile("s_waitcnt vmcnt(0)" ::: "memory");
;             const unsigned og = xb_add(&bar[XB_TOP], 1u);
;             const unsigned tg = og / nx;
;             if (og + 1u == (tg + 1u) * nx) xb_add(&bar[XB_TOPGEN], 1u);
;             else XB_SPIN(xb_ld(&bar[XB_TOPGEN]) == tg, bar);
;             __builtin_amdgcn_fence(__ATOMIC_ACQUIRE, "agent");
;             xb_add(&bar[XB_XGEN(b.x)], 1u);
;             asm volatile("s_waitcnt vmcnt(0)" ::: "memory");
;         } else {
;             XB_SPIN(xb_ld(&bar[XB_XGEN(b.x)]) == gen, bar);
.LBB0_1180:
	s_or_b64 exec, exec, s[20:21]
	v_cvt_f32_u32_e32 v5, v3
	s_waitcnt vmcnt(0)
	v_readfirstlane_b32 s18, v4
	v_sub_u32_e32 v4, 0, v3
	v_rcp_iflag_f32_e32 v5, v5
	v_add_u32_e32 v6, s18, v0
	v_mul_f32_e32 v5, 0x4f7ffffe, v5
	v_cvt_u32_f32_e32 v5, v5
	v_mul_lo_u32 v0, v4, v5
	v_mul_hi_u32 v0, v5, v0
	v_add_u32_e32 v0, v5, v0
	v_mul_hi_u32 v0, v6, v0
	v_mul_lo_u32 v4, v0, v3
	v_sub_u32_e32 v4, v6, v4
	v_add_u32_e32 v5, 1, v0
	v_cmp_ge_u32_e32 vcc, v4, v3
	s_nop 1
	v_cndmask_b32_e32 v0, v0, v5, vcc
	v_sub_u32_e32 v5, v4, v3
	v_cndmask_b32_e32 v4, v4, v5, vcc
	v_add_u32_e32 v5, 1, v0
	v_cmp_ge_u32_e32 vcc, v4, v3
	v_add_u32_e32 v4, 1, v6
	s_nop 0
	v_cndmask_b32_e32 v0, v0, v5, vcc
	v_mul_lo_u32 v5, v3, v0
	v_add_u32_e32 v3, v5, v3
	v_cmp_ne_u32_e32 vcc, v4, v3
	s_and_saveexec_b64 s[18:19], vcc
	s_xor_b64 s[20:21], exec, s[18:19]
	s_cbranch_execz .LBB0_1194
	s_waitcnt lgkmcnt(0)
	buffer_inv sc1
	v_mov_b32_e32 v2, 0x2000
	global_load_dword v2, v2, s[16:17] offset:1024 sc1
	s_add_u32 s18, s16, 0x2400
	s_addc_u32 s19, s17, 0
	s_waitcnt vmcnt(0)
	v_cmp_eq_u32_e32 vcc, v2, v0
	s_and_saveexec_b64 s[22:23], vcc
	s_cbranch_execz .LBB0_1193
	s_mov_b32 s39, 1
	s_mov_b64 s[24:25], 0
	s_branch .LBB0_1184

; __device__ __forceinline__ unsigned xb_ld(unsigned* p)              { return __hip_atomic_load(p, __ATOMIC_RELAXED, __HIP_MEMORY_SCOPE_AGENT); }
; __device__ __forceinline__ unsigned xb_add(unsigned* p, unsigned v) { return __hip_atomic_fetch_add(p, v, __ATOMIC_RELAXED, __HIP_MEMORY_SCOPE_AGENT); }
; #define XB_SPIN(cond, bar) do { unsigned _sp = 0; while (cond) { __builtin_amdgcn_s_sleep(1); \
;     if ((++_sp & 255u) == 0u) { if (xb_ld(&(bar)[XB_TMO])) break; if (_sp > XB_SPIN_CAP) { atomicAdd(&(bar)[XB_TMO], 1u); break; } } } } while (0)
; __device__ __forceinline__ void xcd_barrier(const XcdBarrier& b) {
;     ...
;         if (old + 1u == (gen + 1u) * nloc) {
;             __builtin_amdgcn_fence(__ATOMIC_RELEASE, "agent");
;             asm volatile("s_waitcnt vmcnt(0)" ::: "memory");
;             const unsigned og = xb_add(&bar[XB_TOP], 1u);
;             const unsigned tg = og / nx;
;             if (og + 1u == (tg + 1u) * nx) xb_add(&bar[XB_TOPGEN], 1u);
;             else XB_SPIN(xb_ld(&bar[XB_TOPGEN]) == tg, bar);
;             __builtin_amdgcn_fence(__ATOMIC_ACQUIRE, "agent");
;             xb_add(&bar[XB_XGEN(b.x)], 1u);
;             asm volatile("s_waitcnt vmcnt(0)" ::: "memory");
;         } else {
;             XB_SPIN(xb_ld(&bar[XB_XGEN(b.x)]) == gen, bar);
;             __builtin_amdgcn_fence(__ATOMIC_ACQUIRE, "agent");
.LBB0_1193:
	s_or_b64 exec, exec, s[22:23]
	s_waitcnt vmcnt(0)
	s_waitcnt vmcnt(0)
.LBB0_1194:
	s_andn2_saveexec_b64 s[18:19], s[20:21]
	s_cbranch_execz .LBB0_1214
	s_mov_b64 s[18:19], exec
	buffer_wbl2 sc1
	s_waitcnt lgkmcnt(0)
	s_waitcnt vmcnt(0)
	buffer_inv sc1
	v_mbcnt_lo_u32_b32 v0, s18, 0
	v_mbcnt_hi_u32_b32 v0, s19, v0
	v_cmp_eq_u32_e32 vcc, 0, v0
	s_and_saveexec_b64 s[20:21], vcc
	s_cbranch_execz .LBB0_1197
	s_bcnt1_i32_b64 s18, s[18:19]
	v_mov_b32_e32 v3, s18
	v_mov_b32_e32 v4, 0x3000
	global_atomic_add v3, v4, v3, s[14:15] offset:1024 sc0

; __device__ __forceinline__ unsigned xb_ld(unsigned* p)              { return __hip_atomic_load(p, __ATOMIC_RELAXED, __HIP_MEMORY_SCOPE_AGENT); }
; __device__ __forceinline__ unsigned xb_add(unsigned* p, unsigned v) { return __hip_atomic_fetch_add(p, v, __ATOMIC_RELAXED, __HIP_MEMORY_SCOPE_AGENT); }
; #define XB_SPIN(cond, bar) do { unsigned _sp = 0; while (cond) { __builtin_amdgcn_s_sleep(1); \
;     if ((++_sp & 255u) == 0u) { if (xb_ld(&(bar)[XB_TMO])) break; if (_sp > XB_SPIN_CAP) { atomicAdd(&(bar)[XB_TMO], 1u); break; } } } } while (0)
; __device__ __forceinline__ void xcd_barrier(const XcdBarrier& b) {
;     ...
;             const unsigned og = xb_add(&bar[XB_TOP], 1u);
;             const unsigned tg = og / nx;
;             if (og + 1u == (tg + 1u) * nx) xb_add(&bar[XB_TOPGEN], 1u);
;             else XB_SPIN(xb_ld(&bar[XB_TOPGEN]) == tg, bar);
;             __builtin_amdgcn_fence(__ATOMIC_ACQUIRE, "agent");
;             xb_add(&bar[XB_XGEN(b.x)], 1u);
.LBB0_1211:
	s_or_b64 exec, exec, s[14:15]
	s_mov_b64 s[14:15], exec
	v_mbcnt_lo_u32_b32 v0, s14, 0
	v_mbcnt_hi_u32_b32 v0, s15, v0
	v_cmp_eq_u32_e32 vcc, 0, v0
	s_waitcnt vmcnt(0)
	s_and_saveexec_b64 s[18:19], vcc
	s_cbranch_execz .LBB0_1213
	s_bcnt1_i32_b64 s14, s[14:15]
	v_mov_b32_e32 v0, s14
	v_mov_b32_e32 v2, 0x2000
	global_atomic_add v2, v0, s[16:17] offset:1024

; __device__ __forceinline__ unsigned xb_ld(unsigned* p)              { return __hip_atomic_load(p, __ATOMIC_RELAXED, __HIP_MEMORY_SCOPE_AGENT); }
; __device__ __forceinline__ unsigned xb_add(unsigned* p, unsigned v) { return __hip_atomic_fetch_add(p, v, __ATOMIC_RELAXED, __HIP_MEMORY_SCOPE_AGENT); }
; #define XB_SPIN(cond, bar) do { unsigned _sp = 0; while (cond) { __builtin_amdgcn_s_sleep(1); \
;     if ((++_sp & 255u) == 0u) { if (xb_ld(&(bar)[XB_TMO])) break; if (_sp > XB_SPIN_CAP) { atomicAdd(&(bar)[XB_TMO], 1u); break; } } } } while (0)
; __device__ __forceinline__ void xcd_barrier(const XcdBarrier& b) {
;     ...
;         unsigned nloc = b.st[0], nx = b.st[1];
;         if (nloc == 0u) { xcd_barrier_complete(bar, b.x, nloc, nx); b.st[0] = nloc; b.st[1] = nx; }
;         const unsigned old = xb_add(&bar[XB_XSUB(b.x)], 1u);
;         const unsigned gen = old / nloc;
;         if (old + 1u == (gen + 1u) * nloc) {
;             __builtin_amdgcn_fence(__ATOMIC_RELEASE, "agent");
;             asm volatile("s_waitcnt vmcnt(0)" ::: "memory");
;             const unsigned og = xb_add(&bar[XB_TOP], 1u);
;             const unsigned tg = og / nx;
;             if (og + 1u == (tg + 1u) * nx) xb_add(&bar[XB_TOPGEN], 1u);
;             else XB_SPIN(xb_ld(&bar[XB_TOPGEN]) == tg, bar);
;             __builtin_amdgcn_fence(__ATOMIC_ACQUIRE, "agent");
;             xb_add(&bar[XB_XGEN(b.x)], 1u);
;             asm volatile("s_waitcnt vmcnt(0)" ::: "memory");
;         } else {
;             XB_SPIN(xb_ld(&bar[XB_XGEN(b.x)]) == gen, bar);
.LBB0_1514:
	s_or_b64 exec, exec, s[22:23]
	v_cvt_f32_u32_e32 v5, v3
	s_waitcnt vmcnt(0)
	v_readfirstlane_b32 s18, v4
	v_sub_u32_e32 v4, 0, v3
	v_rcp_iflag_f32_e32 v5, v5
	v_add_u32_e32 v6, s18, v0
	v_mul_f32_e32 v5, 0x4f7ffffe, v5
	v_cvt_u32_f32_e32 v5, v5
	v_mul_lo_u32 v0, v4, v5
	v_mul_hi_u32 v0, v5, v0
	v_add_u32_e32 v0, v5, v0
	v_mul_hi_u32 v0, v6, v0
	v_mul_lo_u32 v4, v0, v3
	v_sub_u32_e32 v4, v6, v4
	v_add_u32_e32 v5, 1, v0
	v_cmp_ge_u32_e32 vcc, v4, v3
	s_nop 1
	v_cndmask_b32_e32 v0, v0, v5, vcc
	v_sub_u32_e32 v5, v4, v3
	v_cndmask_b32_e32 v4, v4, v5, vcc
	v_add_u32_e32 v5, 1, v0
	v_cmp_ge_u32_e32 vcc, v4, v3
	v_add_u32_e32 v4, 1, v6
	s_nop 0
	v_cndmask_b32_e32 v0, v0, v5, vcc
	v_mul_lo_u32 v5, v3, v0
	v_add_u32_e32 v3, v5, v3
	v_cmp_ne_u32_e32 vcc, v4, v3
	s_and_saveexec_b64 s[18:19], vcc
	s_xor_b64 s[22:23], exec, s[18:19]
	s_cbranch_execz .LBB0_1528
	s_waitcnt lgkmcnt(0)
	buffer_inv sc1
	v_mov_b32_e32 v2, 0x2000
	global_load_dword v2, v2, s[20:21] offset:1024 sc1
	s_add_u32 s18, s20, 0x2400
	s_addc_u32 s19, s21, 0
	s_waitcnt vmcnt(0)
	v_cmp_eq_u32_e32 vcc, v2, v0
	s_and_saveexec_b64 s[24:25], vcc
	s_cbranch_execz .LBB0_1527
	s_mov_b32 s41, 1
	s_mov_b64 s[26:27], 0
	s_branch .LBB0_1518

; __device__ __forceinline__ unsigned xb_ld(unsigned* p)              { return __hip_atomic_load(p, __ATOMIC_RELAXED, __HIP_MEMORY_SCOPE_AGENT); }
; __device__ __forceinline__ unsigned xb_add(unsigned* p, unsigned v) { return __hip_atomic_fetch_add(p, v, __ATOMIC_RELAXED, __HIP_MEMORY_SCOPE_AGENT); }
; #define XB_SPIN(cond, bar) do { unsigned _sp = 0; while (cond) { __builtin_amdgcn_s_sleep(1); \
;     if ((++_sp & 255u) == 0u) { if (xb_ld(&(bar)[XB_TMO])) break; if (_sp > XB_SPIN_CAP) { atomicAdd(&(bar)[XB_TMO], 1u); break; } } } } while (0)
; __device__ __forceinline__ void xcd_barrier(const XcdBarrier& b) {
;     ...
;         if (old + 1u == (gen + 1u) * nloc) {
;             __builtin_amdgcn_fence(__ATOMIC_RELEASE, "agent");
;             asm volatile("s_waitcnt vmcnt(0)" ::: "memory");
;             const unsigned og = xb_add(&bar[XB_TOP], 1u);
;             const unsigned tg = og / nx;
;             if (og + 1u == (tg + 1u) * nx) xb_add(&bar[XB_TOPGEN], 1u);
;             else XB_SPIN(xb_ld(&bar[XB_TOPGEN]) == tg, bar);
;             __builtin_amdgcn_fence(__ATOMIC_ACQUIRE, "agent");
;             xb_add(&bar[XB_XGEN(b.x)], 1u);
;             asm volatile("s_waitcnt vmcnt(0)" ::: "memory");
;         } else {
;             XB_SPIN(xb_ld(&bar[XB_XGEN(b.x)]) == gen, bar);
;             __builtin_amdgcn_fence(__ATOMIC_ACQUIRE, "agent");
.LBB0_1527:
	s_or_b64 exec, exec, s[24:25]
	s_waitcnt vmcnt(0)
	s_waitcnt vmcnt(0)
.LBB0_1528:
	s_andn2_saveexec_b64 s[18:19], s[22:23]
	s_cbranch_execz .LBB0_1548
	s_mov_b64 s[18:19], exec
	buffer_wbl2 sc1
	s_waitcnt lgkmcnt(0)
	s_waitcnt vmcnt(0)
	buffer_inv sc1
	v_mbcnt_lo_u32_b32 v0, s18, 0
	v_mbcnt_hi_u32_b32 v0, s19, v0
	v_cmp_eq_u32_e32 vcc, 0, v0
	s_and_saveexec_b64 s[22:23], vcc
	s_cbranch_execz .LBB0_1531
	s_bcnt1_i32_b64 s18, s[18:19]
	v_mov_b32_e32 v3, s18
	v_mov_b32_e32 v4, 0x3000
	global_atomic_add v3, v4, v3, s[16:17] offset:1024 sc0

; __device__ __forceinline__ unsigned xb_ld(unsigned* p)              { return __hip_atomic_load(p, __ATOMIC_RELAXED, __HIP_MEMORY_SCOPE_AGENT); }
; __device__ __forceinline__ unsigned xb_add(unsigned* p, unsigned v) { return __hip_atomic_fetch_add(p, v, __ATOMIC_RELAXED, __HIP_MEMORY_SCOPE_AGENT); }
; #define XB_SPIN(cond, bar) do { unsigned _sp = 0; while (cond) { __builtin_amdgcn_s_sleep(1); \
;     if ((++_sp & 255u) == 0u) { if (xb_ld(&(bar)[XB_TMO])) break; if (_sp > XB_SPIN_CAP) { atomicAdd(&(bar)[XB_TMO], 1u); break; } } } } while (0)
; __device__ __forceinline__ void xcd_barrier(const XcdBarrier& b) {
;     ...
;             const unsigned og = xb_add(&bar[XB_TOP], 1u);
;             const unsigned tg = og / nx;
;             if (og + 1u == (tg + 1u) * nx) xb_add(&bar[XB_TOPGEN], 1u);
;             else XB_SPIN(xb_ld(&bar[XB_TOPGEN]) == tg, bar);
;             __builtin_amdgcn_fence(__ATOMIC_ACQUIRE, "agent");
;             xb_add(&bar[XB_XGEN(b.x)], 1u);
.LBB0_1545:
	s_or_b64 exec, exec, s[16:17]
	s_mov_b64 s[16:17], exec
	v_mbcnt_lo_u32_b32 v0, s16, 0
	v_mbcnt_hi_u32_b32 v0, s17, v0
	v_cmp_eq_u32_e32 vcc, 0, v0
	s_waitcnt vmcnt(0)
	s_and_saveexec_b64 s[18:19], vcc
	s_cbranch_execz .LBB0_1547
	s_bcnt1_i32_b64 s16, s[16:17]
	v_mov_b32_e32 v0, s16
	v_mov_b32_e32 v2, 0x2000
	global_atomic_add v2, v0, s[20:21] offset:1024

; __device__ __forceinline__ unsigned xb_ld(unsigned* p)              { return __hip_atomic_load(p, __ATOMIC_RELAXED, __HIP_MEMORY_SCOPE_AGENT); }
; __device__ __forceinline__ unsigned xb_add(unsigned* p, unsigned v) { return __hip_atomic_fetch_add(p, v, __ATOMIC_RELAXED, __HIP_MEMORY_SCOPE_AGENT); }
; #define XB_SPIN(cond, bar) do { unsigned _sp = 0; while (cond) { __builtin_amdgcn_s_sleep(1); \
;     if ((++_sp & 255u) == 0u) { if (xb_ld(&(bar)[XB_TMO])) break; if (_sp > XB_SPIN_CAP) { atomicAdd(&(bar)[XB_TMO], 1u); break; } } } } while (0)
; __device__ __forceinline__ void xcd_barrier(const XcdBarrier& b) {
;     ...
;         unsigned nloc = b.st[0], nx = b.st[1];
;         if (nloc == 0u) { xcd_barrier_complete(bar, b.x, nloc, nx); b.st[0] = nloc; b.st[1] = nx; }
;         const unsigned old = xb_add(&bar[XB_XSUB(b.x)], 1u);
;         const unsigned gen = old / nloc;
;         if (old + 1u == (gen + 1u) * nloc) {
;             __builtin_amdgcn_fence(__ATOMIC_RELEASE, "agent");
;             asm volatile("s_waitcnt vmcnt(0)" ::: "memory");
;             const unsigned og = xb_add(&bar[XB_TOP], 1u);
;             const unsigned tg = og / nx;
;             if (og + 1u == (tg + 1u) * nx) xb_add(&bar[XB_TOPGEN], 1u);
;             else XB_SPIN(xb_ld(&bar[XB_TOPGEN]) == tg, bar);
;             __builtin_amdgcn_fence(__ATOMIC_ACQUIRE, "agent");
;             xb_add(&bar[XB_XGEN(b.x)], 1u);
;             asm volatile("s_waitcnt vmcnt(0)" ::: "memory");
;         } else {
;             XB_SPIN(xb_ld(&bar[XB_XGEN(b.x)]) == gen, bar);
.LBB0_1648:
	s_or_b64 exec, exec, s[20:21]
	v_cvt_f32_u32_e32 v5, v3
	s_waitcnt vmcnt(0)
	v_readfirstlane_b32 s18, v4
	v_sub_u32_e32 v4, 0, v3
	v_rcp_iflag_f32_e32 v5, v5
	v_add_u32_e32 v6, s18, v0
	v_mul_f32_e32 v5, 0x4f7ffffe, v5
	v_cvt_u32_f32_e32 v5, v5
	v_mul_lo_u32 v0, v4, v5
	v_mul_hi_u32 v0, v5, v0
	v_add_u32_e32 v0, v5, v0
	v_mul_hi_u32 v0, v6, v0
	v_mul_lo_u32 v4, v0, v3
	v_sub_u32_e32 v4, v6, v4
	v_add_u32_e32 v5, 1, v0
	v_cmp_ge_u32_e32 vcc, v4, v3
	s_nop 1
	v_cndmask_b32_e32 v0, v0, v5, vcc
	v_sub_u32_e32 v5, v4, v3
	v_cndmask_b32_e32 v4, v4, v5, vcc
	v_add_u32_e32 v5, 1, v0
	v_cmp_ge_u32_e32 vcc, v4, v3
	v_add_u32_e32 v4, 1, v6
	s_nop 0
	v_cndmask_b32_e32 v0, v0, v5, vcc
	v_mul_lo_u32 v5, v3, v0
	v_add_u32_e32 v3, v5, v3
	v_cmp_ne_u32_e32 vcc, v4, v3
	s_and_saveexec_b64 s[18:19], vcc
	s_xor_b64 s[20:21], exec, s[18:19]
	s_cbranch_execz .LBB0_1662
	s_waitcnt lgkmcnt(0)
	buffer_inv sc1
	v_mov_b32_e32 v2, 0x2000
	global_load_dword v2, v2, s[16:17] offset:1024 sc1
	s_add_u32 s18, s16, 0x2400
	s_addc_u32 s19, s17, 0
	s_waitcnt vmcnt(0)
	v_cmp_eq_u32_e32 vcc, v2, v0
	s_and_saveexec_b64 s[22:23], vcc
	s_cbranch_execz .LBB0_1661
	s_mov_b32 s38, 1
	s_mov_b64 s[24:25], 0
	s_branch .LBB0_1652

; __device__ __forceinline__ unsigned xb_ld(unsigned* p)              { return __hip_atomic_load(p, __ATOMIC_RELAXED, __HIP_MEMORY_SCOPE_AGENT); }
; __device__ __forceinline__ unsigned xb_add(unsigned* p, unsigned v) { return __hip_atomic_fetch_add(p, v, __ATOMIC_RELAXED, __HIP_MEMORY_SCOPE_AGENT); }
; #define XB_SPIN(cond, bar) do { unsigned _sp = 0; while (cond) { __builtin_amdgcn_s_sleep(1); \
;     if ((++_sp & 255u) == 0u) { if (xb_ld(&(bar)[XB_TMO])) break; if (_sp > XB_SPIN_CAP) { atomicAdd(&(bar)[XB_TMO], 1u); break; } } } } while (0)
; __device__ __forceinline__ void xcd_barrier(const XcdBarrier& b) {
;     ...
;         unsigned nloc = b.st[0], nx = b.st[1];
;         if (nloc == 0u) { xcd_barrier_complete(bar, b.x, nloc, nx); b.st[0] = nloc; b.st[1] = nx; }
;         const unsigned old = xb_add(&bar[XB_XSUB(b.x)], 1u);
;         const unsigned gen = old / nloc;
;         if (old + 1u == (gen + 1u) * nloc) {
;             __builtin_amdgcn_fence(__ATOMIC_RELEASE, "agent");
;             asm volatile("s_waitcnt vmcnt(0)" ::: "memory");
;             const unsigned og = xb_add(&bar[XB_TOP], 1u);
;             const unsigned tg = og / nx;
;             if (og + 1u == (tg + 1u) * nx) xb_add(&bar[XB_TOPGEN], 1u);
;             else XB_SPIN(xb_ld(&bar[XB_TOPGEN]) == tg, bar);
;             __builtin_amdgcn_fence(__ATOMIC_ACQUIRE, "agent");
;             xb_add(&bar[XB_XGEN(b.x)], 1u);
;             asm volatile("s_waitcnt vmcnt(0)" ::: "memory");
;         } else {
;             XB_SPIN(xb_ld(&bar[XB_XGEN(b.x)]) == gen, bar);
.LBB0_2116:
	s_or_b64 exec, exec, s[24:25]
	v_cvt_f32_u32_e32 v5, v3
	s_waitcnt vmcnt(0)
	v_readfirstlane_b32 s18, v4
	v_sub_u32_e32 v4, 0, v3
	v_rcp_iflag_f32_e32 v5, v5
	v_add_u32_e32 v6, s18, v0
	v_mul_f32_e32 v5, 0x4f7ffffe, v5
	v_cvt_u32_f32_e32 v5, v5
	v_mul_lo_u32 v0, v4, v5
	v_mul_hi_u32 v0, v5, v0
	v_add_u32_e32 v0, v5, v0
	v_mul_hi_u32 v0, v6, v0
	v_mul_lo_u32 v4, v0, v3
	v_sub_u32_e32 v4, v6, v4
	v_add_u32_e32 v5, 1, v0
	v_cmp_ge_u32_e32 vcc, v4, v3
	s_nop 1
	v_cndmask_b32_e32 v0, v0, v5, vcc
	v_sub_u32_e32 v5, v4, v3
	v_cndmask_b32_e32 v4, v4, v5, vcc
	v_add_u32_e32 v5, 1, v0
	v_cmp_ge_u32_e32 vcc, v4, v3
	v_add_u32_e32 v4, 1, v6
	s_nop 0
	v_cndmask_b32_e32 v0, v0, v5, vcc
	v_mul_lo_u32 v5, v3, v0
	v_add_u32_e32 v3, v5, v3
	v_cmp_ne_u32_e32 vcc, v4, v3
	s_and_saveexec_b64 s[18:19], vcc
	s_xor_b64 s[24:25], exec, s[18:19]
	s_cbranch_execz .LBB0_2130
	s_waitcnt lgkmcnt(0)
	buffer_inv sc1
	v_mov_b32_e32 v2, 0x2000
	global_load_dword v2, v2, s[22:23] offset:1024 sc1
	s_add_u32 s18, s22, 0x2400
	s_addc_u32 s19, s23, 0
	s_waitcnt vmcnt(0)
	v_cmp_eq_u32_e32 vcc, v2, v0
	s_and_saveexec_b64 s[26:27], vcc
	s_cbranch_execz .LBB0_2129
	s_mov_b32 s41, 1
	s_mov_b64 s[28:29], 0
	s_branch .LBB0_2120

; __device__ __forceinline__ unsigned xb_ld(unsigned* p)              { return __hip_atomic_load(p, __ATOMIC_RELAXED, __HIP_MEMORY_SCOPE_AGENT); }
; __device__ __forceinline__ unsigned xb_add(unsigned* p, unsigned v) { return __hip_atomic_fetch_add(p, v, __ATOMIC_RELAXED, __HIP_MEMORY_SCOPE_AGENT); }
; #define XB_SPIN(cond, bar) do { unsigned _sp = 0; while (cond) { __builtin_amdgcn_s_sleep(1); \
;     if ((++_sp & 255u) == 0u) { if (xb_ld(&(bar)[XB_TMO])) break; if (_sp > XB_SPIN_CAP) { atomicAdd(&(bar)[XB_TMO], 1u); break; } } } } while (0)
; __device__ __forceinline__ void xcd_barrier(const XcdBarrier& b) {
;     ...
;         if (old + 1u == (gen + 1u) * nloc) {
;             __builtin_amdgcn_fence(__ATOMIC_RELEASE, "agent");
;             asm volatile("s_waitcnt vmcnt(0)" ::: "memory");
;             const unsigned og = xb_add(&bar[XB_TOP], 1u);
;             const unsigned tg = og / nx;
;             if (og + 1u == (tg + 1u) * nx) xb_add(&bar[XB_TOPGEN], 1u);
;             else XB_SPIN(xb_ld(&bar[XB_TOPGEN]) == tg, bar);
;             __builtin_amdgcn_fence(__ATOMIC_ACQUIRE, "agent");
;             xb_add(&bar[XB_XGEN(b.x)], 1u);
;             asm volatile("s_waitcnt vmcnt(0)" ::: "memory");
;         } else {
;             XB_SPIN(xb_ld(&bar[XB_XGEN(b.x)]) == gen, bar);
;             __builtin_amdgcn_fence(__ATOMIC_ACQUIRE, "agent");
.LBB0_2129:
	s_or_b64 exec, exec, s[26:27]
	s_waitcnt vmcnt(0)
	s_waitcnt vmcnt(0)
.LBB0_2130:
	s_andn2_saveexec_b64 s[18:19], s[24:25]
	s_cbranch_execz .LBB0_2150
	s_mov_b64 s[18:19], exec
	buffer_wbl2 sc1
	s_waitcnt lgkmcnt(0)
	s_waitcnt vmcnt(0)
	buffer_inv sc1
	v_mbcnt_lo_u32_b32 v0, s18, 0
	v_mbcnt_hi_u32_b32 v0, s19, v0
	v_cmp_eq_u32_e32 vcc, 0, v0
	s_and_saveexec_b64 s[24:25], vcc
	s_cbranch_execz .LBB0_2133
	s_bcnt1_i32_b64 s18, s[18:19]
	v_mov_b32_e32 v3, s18
	v_mov_b32_e32 v4, 0x3000
	global_atomic_add v3, v4, v3, s[20:21] offset:1024 sc0

; __device__ __forceinline__ unsigned xb_ld(unsigned* p)              { return __hip_atomic_load(p, __ATOMIC_RELAXED, __HIP_MEMORY_SCOPE_AGENT); }
; __device__ __forceinline__ unsigned xb_add(unsigned* p, unsigned v) { return __hip_atomic_fetch_add(p, v, __ATOMIC_RELAXED, __HIP_MEMORY_SCOPE_AGENT); }
; #define XB_SPIN(cond, bar) do { unsigned _sp = 0; while (cond) { __builtin_amdgcn_s_sleep(1); \
;     if ((++_sp & 255u) == 0u) { if (xb_ld(&(bar)[XB_TMO])) break; if (_sp > XB_SPIN_CAP) { atomicAdd(&(bar)[XB_TMO], 1u); break; } } } } while (0)
; __device__ __forceinline__ void xcd_barrier(const XcdBarrier& b) {
;     ...
;             const unsigned og = xb_add(&bar[XB_TOP], 1u);
;             const unsigned tg = og / nx;
;             if (og + 1u == (tg + 1u) * nx) xb_add(&bar[XB_TOPGEN], 1u);
;             else XB_SPIN(xb_ld(&bar[XB_TOPGEN]) == tg, bar);
;             __builtin_amdgcn_fence(__ATOMIC_ACQUIRE, "agent");
;             xb_add(&bar[XB_XGEN(b.x)], 1u);
.LBB0_2147:
	s_or_b64 exec, exec, s[20:21]
	s_mov_b64 s[18:19], exec
	v_mbcnt_lo_u32_b32 v0, s18, 0
	v_mbcnt_hi_u32_b32 v0, s19, v0
	v_cmp_eq_u32_e32 vcc, 0, v0
	s_waitcnt vmcnt(0)
	s_and_saveexec_b64 s[20:21], vcc
	s_cbranch_execz .LBB0_2149
	s_bcnt1_i32_b64 s18, s[18:19]
	v_mov_b32_e32 v0, s18
	v_mov_b32_e32 v2, 0x2000
	global_atomic_add v2, v0, s[22:23] offset:1024

; #define GAS __attribute__((address_space(1)))
; __device__ __forceinline__ f32x4 bf4_to_f32(u32x2_g a) { return (f32x4){__uint_as_float(a.x << 16), __uint_as_float(a.x & 0xffff0000u), __uint_as_float(a.y << 16), __uint_as_float(a.y & 0xffff0000u)}; }
; #define lane (lane_id())
; __device__ __forceinline__ void combine_phase(const Ptrs& P, int vcu, int G, int wave, int lane) {
;     ...
;     for (int m0 = gw; m0 < M; m0 += 2 * NGW) {
;         const int m1 = m0 + NGW; const bool has1 = m1 < M; const int mm[2] = {m0, has1 ? m1 : m0};
;         int pa[2], pb[2]; float ga[2], gb[2];
; #pragma unroll
;         for (int q = 0; q < 2; ++q) { pa[q] = P.sel_pos[2 * mm[q]]; pb[q] = P.sel_pos[2 * mm[q] + 1]; ga[q] = P.sel_g[2 * mm[q]]; gb[q] = P.sel_g[2 * mm[q] + 1]; }
;         f32x4 ya[2][8], yb[2][8], hv[2][8];
; #pragma unroll
;         for (int q = 0; q < 2; ++q) { const GAS u32x2_t* y0 = (const GAS u32x2_t*)(P.YS + (size_t)pa[q] * D) + lane; const GAS u32x2_t* y1 = (const GAS u32x2_t*)(P.YS + (size_t)pb[q] * D) + lane;
;             const GAS u32x2_g* hr = (const GAS u32x2_g*)(P.H + (size_t)mm[q] * D) + lane;
; #pragma unroll
;             for (int j = 0; j < 8; ++j) { ya[q][j] = bf4_to_f32(y0[64 * j]); yb[q][j] = bf4_to_f32(y1[64 * j]); hv[q][j] = bf4_to_f32(hr[64 * j]); } }
; #pragma unroll
;         for (int q = 0; q < 2; ++q) { if (q == 1 && !has1) break;
.LBB0_2157:
	s_add_i32 s15, s68, s30
	s_cmpk_lt_i32 s15, 0x2000
	s_cselect_b64 s[22:23], -1, 0
	s_and_b64 s[16:17], s[22:23], exec
	s_cselect_b32 s16, s15, s30
	s_ashr_i32 s15, s14, 31
	s_lshl_b64 s[20:21], s[14:15], 2
	s_add_u32 s24, s28, s20
	s_addc_u32 s25, s29, s21
	global_load_dwordx2 v[114:115], v1, s[24:25]
	s_add_u32 s20, s18, s20
	s_addc_u32 s21, s19, s21
	s_lshl_b32 s24, s16, 1
	s_ashr_i32 s25, s24, 31
	s_lshl_b64 s[24:25], s[24:25], 2
	s_add_u32 s26, s28, s24
	s_addc_u32 s27, s29, s25
	global_load_dwordx2 v[132:133], v1, s[26:27]
	global_load_dwordx2 v[80:81], v[12:13], off offset:-2048
	global_load_dwordx2 v[78:79], v[12:13], off offset:-1536
	global_load_dwordx2 v[76:77], v[12:13], off offset:-1024
	global_load_dwordx2 v[74:75], v[12:13], off offset:-512
	global_load_dwordx2 v[72:73], v[12:13], off
	global_load_dwordx2 v[70:71], v[12:13], off offset:512
	global_load_dwordx2 v[68:69], v[12:13], off offset:1024
	global_load_dwordx2 v[66:67], v[12:13], off offset:1536
	s_add_u32 s24, s18, s24
	s_addc_u32 s25, s19, s25
	s_ashr_i32 s17, s16, 31
	global_load_dwordx2 v[14:15], v1, s[24:25]
	global_load_dwordx2 v[48:49], v1, s[20:21]
	s_lshl_b64 s[20:21], s[16:17], 12
	v_lshl_add_u64 v[30:31], v[4:5], 0, s[20:21]
	global_load_dwordx2 v[16:17], v[30:31], off
	global_load_dwordx2 v[18:19], v[30:31], off offset:512
	global_load_dwordx2 v[20:21], v[30:31], off offset:1024
	global_load_dwordx2 v[22:23], v[30:31], off offset:1536
	global_load_dwordx2 v[24:25], v[30:31], off offset:2048
	global_load_dwordx2 v[26:27], v[30:31], off offset:2560
	global_load_dwordx2 v[28:29], v[30:31], off offset:3072
	s_nop 0
	global_load_dwordx2 v[30:31], v[30:31], off offset:3584
	s_waitcnt vmcnt(18)
	v_readfirstlane_b32 s24, v132
	v_readfirstlane_b32 s26, v114
	v_ashrrev_i32_e32 v33, 31, v115
	v_mov_b32_e32 v32, v115
	s_ashr_i32 s27, s26, 31
	v_lshlrev_b64 v[32:33], 12, v[32:33]
	s_lshl_b64 s[20:21], s[26:27], 12
	v_lshl_add_u64 v[32:33], v[2:3], 0, v[32:33]
	v_lshl_add_u64 v[34:35], v[2:3], 0, s[20:21]
	global_load_dwordx2 v[130:131], v[32:33], off
	global_load_dwordx2 v[128:129], v[32:33], off offset:512
	global_load_dwordx2 v[126:127], v[32:33], off offset:1024
	global_load_dwordx2 v[124:125], v[32:33], off offset:1536
	global_load_dwordx2 v[82:83], v[34:35], off
	global_load_dwordx2 v[84:85], v[34:35], off offset:512
	global_load_dwordx2 v[122:123], v[32:33], off offset:2048
	global_load_dwordx2 v[120:121], v[32:33], off offset:2560
	global_load_dwordx2 v[118:119], v[32:33], off offset:3072
	global_load_dwordx2 v[116:117], v[32:33], off offset:3584
	global_load_dwordx2 v[86:87], v[34:35], off offset:1024
	global_load_dwordx2 v[88:89], v[34:35], off offset:1536
	global_load_dwordx2 v[90:91], v[34:35], off offset:2048
	global_load_dwordx2 v[134:135], v[34:35], off offset:2560
	global_load_dwordx2 v[136:137], v[34:35], off offset:3072
	global_load_dwordx2 v[138:139], v[34:35], off offset:3584
	v_ashrrev_i32_e32 v33, 31, v132
	v_mov_b32_e32 v32, v132
	v_ashrrev_i32_e32 v35, 31, v133
	v_mov_b32_e32 v34, v133
	v_lshlrev_b64 v[32:33], 12, v[32:33]
	v_lshlrev_b64 v[34:35], 12, v[34:35]
	v_lshl_add_u64 v[32:33], v[2:3], 0, v[32:33]
	v_lshl_add_u64 v[92:93], v[2:3], 0, v[34:35]
	global_load_dwordx2 v[64:65], v[32:33], off
	global_load_dwordx2 v[62:63], v[32:33], off offset:512
	global_load_dwordx2 v[60:61], v[32:33], off offset:1024
	global_load_dwordx2 v[58:59], v[32:33], off offset:1536
	global_load_dwordx2 v[46:47], v[92:93], off
	global_load_dwordx2 v[44:45], v[92:93], off offset:512
	global_load_dwordx2 v[42:43], v[92:93], off offset:1024
	global_load_dwordx2 v[38:39], v[92:93], off offset:1536
	global_load_dwordx2 v[56:57], v[32:33], off offset:2048
	global_load_dwordx2 v[54:55], v[32:33], off offset:2560
	global_load_dwordx2 v[52:53], v[32:33], off offset:3072
	global_load_dwordx2 v[50:51], v[32:33], off offset:3584
	global_load_dwordx2 v[40:41], v[92:93], off offset:2048
	global_load_dwordx2 v[36:37], v[92:93], off offset:2560
	global_load_dwordx2 v[34:35], v[92:93], off offset:3072
	s_nop 0
	global_load_dwordx2 v[32:33], v[92:93], off offset:3584
	s_cmpk_lt_i32 s26, 0x4000
	v_readfirstlane_b32 s20, v133
	s_waitcnt vmcnt(27)
	v_lshlrev_b32_e32 v112, 16, v82
	v_and_b32_e32 v113, 0xffff0000, v82
	v_lshlrev_b32_e32 v110, 16, v83
	v_and_b32_e32 v111, 0xffff0000, v83
	s_waitcnt vmcnt(26)
	v_lshlrev_b32_e32 v108, 16, v84
	v_and_b32_e32 v109, 0xffff0000, v84
	v_lshlrev_b32_e32 v106, 16, v85
	v_and_b32_e32 v107, 0xffff0000, v85
	s_waitcnt vmcnt(21)
	v_lshlrev_b32_e32 v104, 16, v86
	v_and_b32_e32 v105, 0xffff0000, v86
	v_lshlrev_b32_e32 v102, 16, v87
	v_and_b32_e32 v103, 0xffff0000, v87
	s_waitcnt vmcnt(20)
	v_lshlrev_b32_e32 v100, 16, v88
	v_and_b32_e32 v101, 0xffff0000, v88
	v_lshlrev_b32_e32 v98, 16, v89
	v_and_b32_e32 v99, 0xffff0000, v89
	s_waitcnt vmcnt(19)
	v_lshlrev_b32_e32 v96, 16, v90
	v_and_b32_e32 v97, 0xffff0000, v90
	v_lshlrev_b32_e32 v94, 16, v91
	v_and_b32_e32 v95, 0xffff0000, v91
	s_waitcnt vmcnt(18)
	v_lshlrev_b32_e32 v92, 16, v134
	v_and_b32_e32 v93, 0xffff0000, v134
	v_lshlrev_b32_e32 v90, 16, v135
	v_and_b32_e32 v91, 0xffff0000, v135
	s_waitcnt vmcnt(17)
	v_lshlrev_b32_e32 v88, 16, v136
	v_and_b32_e32 v89, 0xffff0000, v136
	v_lshlrev_b32_e32 v86, 16, v137
	v_and_b32_e32 v87, 0xffff0000, v137
	s_waitcnt vmcnt(16)
	v_lshlrev_b32_e32 v84, 16, v138
	v_and_b32_e32 v85, 0xffff0000, v138
	v_lshlrev_b32_e32 v82, 16, v139
	v_and_b32_e32 v83, 0xffff0000, v139
	s_cbranch_scc1 .LBB0_2159
; #define GAS __attribute__((address_space(1)))
; __device__ __forceinline__ f32x4 bf4_to_f32(u32x2_g a) { return (f32x4){__uint_as_float(a.x << 16), __uint_as_float(a.x & 0xffff0000u), __uint_as_float(a.y << 16), __uint_as_float(a.y & 0xffff0000u)}; }
; #define lane (lane_id())
; __device__ __forceinline__ void combine_phase(const Ptrs& P, int vcu, int G, int wave, int lane) {
;     ...
;             if (pa[q] >= 16384) { const GAS u32x2_t* z0 = (const GAS u32x2_t*)(P.YS + (size_t)MPAD * D + (size_t)pa[q] * D) + lane;
; #pragma unroll
;                 for (int j = 0; j < 8; ++j) ya[q][j] += bf4_to_f32(z0[64 * j]); }
;             if (pb[q] >= 16384) { const GAS u32x2_t* z1 = (const GAS u32x2_t*)(P.YS + (size_t)MPAD * D + (size_t)pb[q] * D) + lane;
; #pragma unroll
;                 for (int j = 0; j < 8; ++j) yb[q][j] += bf4_to_f32(z1[64 * j]); }
	s_mov_b32 s27, s90
	s_lshl_b64 s[26:27], s[26:27], 12
	v_lshl_add_u64 v[132:133], v[6:7], 0, s[26:27]
	global_load_dwordx2 v[166:167], v[132:133], off
	global_load_dwordx2 v[168:169], v[132:133], off offset:512
	global_load_dwordx2 v[170:171], v[132:133], off offset:1024
	global_load_dwordx2 v[172:173], v[132:133], off offset:1536
	global_load_dwordx2 v[174:175], v[132:133], off offset:2048
	global_load_dwordx2 v[176:177], v[132:133], off offset:2560
	global_load_dwordx2 v[178:179], v[132:133], off offset:3072
	global_load_dwordx2 v[180:181], v[132:133], off offset:3584
	s_waitcnt vmcnt(0)
	v_lshlrev_b32_e32 v136, 16, v166
	v_and_b32_e32 v137, 0xffff0000, v166
	v_lshlrev_b32_e32 v134, 16, v167
	v_and_b32_e32 v135, 0xffff0000, v167
	v_pk_add_f32 v[110:111], v[110:111], v[134:135]
	v_pk_add_f32 v[112:113], v[112:113], v[136:137]
	v_lshlrev_b32_e32 v136, 16, v168
	v_and_b32_e32 v137, 0xffff0000, v168
	v_lshlrev_b32_e32 v134, 16, v169
	v_and_b32_e32 v135, 0xffff0000, v169
	v_pk_add_f32 v[106:107], v[106:107], v[134:135]
	v_pk_add_f32 v[108:109], v[108:109], v[136:137]
	v_lshlrev_b32_e32 v136, 16, v170
	v_and_b32_e32 v137, 0xffff0000, v170
	v_lshlrev_b32_e32 v134, 16, v171
	v_and_b32_e32 v135, 0xffff0000, v171
	v_pk_add_f32 v[102:103], v[102:103], v[134:135]
	v_pk_add_f32 v[104:105], v[104:105], v[136:137]
	v_lshlrev_b32_e32 v136, 16, v172
	v_and_b32_e32 v137, 0xffff0000, v172
	v_lshlrev_b32_e32 v134, 16, v173
	v_and_b32_e32 v135, 0xffff0000, v173
	v_pk_add_f32 v[98:99], v[98:99], v[134:135]
	v_pk_add_f32 v[100:101], v[100:101], v[136:137]
	v_lshlrev_b32_e32 v136, 16, v174
	v_and_b32_e32 v137, 0xffff0000, v174
	v_lshlrev_b32_e32 v134, 16, v175
	v_and_b32_e32 v135, 0xffff0000, v175
	v_pk_add_f32 v[94:95], v[94:95], v[134:135]
	v_pk_add_f32 v[96:97], v[96:97], v[136:137]
	v_lshlrev_b32_e32 v136, 16, v176
	v_and_b32_e32 v137, 0xffff0000, v176
	v_lshlrev_b32_e32 v134, 16, v177
	v_and_b32_e32 v135, 0xffff0000, v177
	v_pk_add_f32 v[90:91], v[90:91], v[134:135]
	v_pk_add_f32 v[92:93], v[92:93], v[136:137]
	v_lshlrev_b32_e32 v136, 16, v178
	v_and_b32_e32 v137, 0xffff0000, v178
	v_lshlrev_b32_e32 v134, 16, v179
	v_and_b32_e32 v135, 0xffff0000, v179
	v_pk_add_f32 v[86:87], v[86:87], v[134:135]
	v_lshlrev_b32_e32 v134, 16, v180
	v_and_b32_e32 v135, 0xffff0000, v180
	v_lshlrev_b32_e32 v132, 16, v181
	v_and_b32_e32 v133, 0xffff0000, v181
	v_pk_add_f32 v[88:89], v[88:89], v[136:137]
	v_pk_add_f32 v[82:83], v[82:83], v[132:133]
	v_pk_add_f32 v[84:85], v[84:85], v[134:135]
.LBB0_2159:
	s_movk_i32 s15, 0x4000
	v_cmp_gt_i32_e32 vcc, s15, v115
	v_lshlrev_b32_e32 v144, 16, v130
	v_and_b32_e32 v145, 0xffff0000, v130
	v_lshlrev_b32_e32 v146, 16, v131
	v_and_b32_e32 v147, 0xffff0000, v131
	v_lshlrev_b32_e32 v140, 16, v128
	v_and_b32_e32 v141, 0xffff0000, v128
	v_lshlrev_b32_e32 v142, 16, v129
	v_and_b32_e32 v143, 0xffff0000, v129
	v_lshlrev_b32_e32 v136, 16, v126
	v_and_b32_e32 v137, 0xffff0000, v126
	v_lshlrev_b32_e32 v138, 16, v127
	v_and_b32_e32 v139, 0xffff0000, v127
	v_lshlrev_b32_e32 v132, 16, v124
	v_and_b32_e32 v133, 0xffff0000, v124
	v_lshlrev_b32_e32 v134, 16, v125
	v_and_b32_e32 v135, 0xffff0000, v125
	v_lshlrev_b32_e32 v128, 16, v122
	v_and_b32_e32 v129, 0xffff0000, v122
	v_lshlrev_b32_e32 v130, 16, v123
	v_and_b32_e32 v131, 0xffff0000, v123
	v_lshlrev_b32_e32 v124, 16, v120
	v_and_b32_e32 v125, 0xffff0000, v120
	v_lshlrev_b32_e32 v126, 16, v121
	v_and_b32_e32 v127, 0xffff0000, v121
	v_lshlrev_b32_e32 v120, 16, v118
	v_and_b32_e32 v121, 0xffff0000, v118
	v_lshlrev_b32_e32 v122, 16, v119
	v_and_b32_e32 v123, 0xffff0000, v119
	v_lshlrev_b32_e32 v118, 16, v116
	v_and_b32_e32 v119, 0xffff0000, v116
	v_lshlrev_b32_e32 v116, 16, v117
	v_and_b32_e32 v117, 0xffff0000, v117
	s_cbranch_vccnz .LBB0_2161
	v_mov_b32_e32 v0, v115
	v_lshlrev_b64 v[114:115], 12, v[0:1]
	v_lshl_add_u64 v[114:115], v[6:7], 0, v[114:115]
	global_load_dwordx2 v[166:167], v[114:115], off
	global_load_dwordx2 v[168:169], v[114:115], off offset:512
	global_load_dwordx2 v[170:171], v[114:115], off offset:1024
	global_load_dwordx2 v[172:173], v[114:115], off offset:1536
	global_load_dwordx2 v[174:175], v[114:115], off offset:2048
	global_load_dwordx2 v[176:177], v[114:115], off offset:2560
	global_load_dwordx2 v[178:179], v[114:115], off offset:3072
	global_load_dwordx2 v[180:181], v[114:115], off offset:3584
	s_waitcnt vmcnt(0)
	v_lshlrev_b32_e32 v150, 16, v166
	v_and_b32_e32 v151, 0xffff0000, v166
	v_lshlrev_b32_e32 v148, 16, v167
	v_and_b32_e32 v149, 0xffff0000, v167
	v_pk_add_f32 v[146:147], v[146:147], v[148:149]
	v_pk_add_f32 v[144:145], v[144:145], v[150:151]
	v_lshlrev_b32_e32 v150, 16, v168
	v_and_b32_e32 v151, 0xffff0000, v168
	v_lshlrev_b32_e32 v148, 16, v169
	v_and_b32_e32 v149, 0xffff0000, v169
	v_pk_add_f32 v[142:143], v[142:143], v[148:149]
	v_pk_add_f32 v[140:141], v[140:141], v[150:151]
	v_lshlrev_b32_e32 v150, 16, v170
	v_and_b32_e32 v151, 0xffff0000, v170
	v_lshlrev_b32_e32 v148, 16, v171
	v_and_b32_e32 v149, 0xffff0000, v171
	v_pk_add_f32 v[138:139], v[138:139], v[148:149]
	v_pk_add_f32 v[136:137], v[136:137], v[150:151]
	v_lshlrev_b32_e32 v150, 16, v172
	v_and_b32_e32 v151, 0xffff0000, v172
	v_lshlrev_b32_e32 v148, 16, v173
	v_and_b32_e32 v149, 0xffff0000, v173
	v_pk_add_f32 v[134:135], v[134:135], v[148:149]
	v_pk_add_f32 v[132:133], v[132:133], v[150:151]
	v_lshlrev_b32_e32 v150, 16, v174
	v_and_b32_e32 v151, 0xffff0000, v174
	v_lshlrev_b32_e32 v148, 16, v175
	v_and_b32_e32 v149, 0xffff0000, v175
	v_pk_add_f32 v[130:131], v[130:131], v[148:149]
	v_pk_add_f32 v[128:129], v[128:129], v[150:151]
	v_lshlrev_b32_e32 v150, 16, v176
	v_and_b32_e32 v151, 0xffff0000, v176
	v_lshlrev_b32_e32 v148, 16, v177
	v_and_b32_e32 v149, 0xffff0000, v177
	v_pk_add_f32 v[126:127], v[126:127], v[148:149]
	v_pk_add_f32 v[124:125], v[124:125], v[150:151]
	v_lshlrev_b32_e32 v150, 16, v178
	v_and_b32_e32 v151, 0xffff0000, v178
	v_lshlrev_b32_e32 v148, 16, v179
	v_and_b32_e32 v149, 0xffff0000, v179
	v_pk_add_f32 v[122:123], v[122:123], v[148:149]
	v_lshlrev_b32_e32 v148, 16, v180
	v_and_b32_e32 v149, 0xffff0000, v180
	v_lshlrev_b32_e32 v114, 16, v181
	v_and_b32_e32 v115, 0xffff0000, v181
	v_pk_add_f32 v[120:121], v[120:121], v[150:151]
	v_pk_add_f32 v[116:117], v[116:117], v[114:115]
	v_pk_add_f32 v[118:119], v[118:119], v[148:149]
; #define GAS __attribute__((address_space(1)))
; #define lane (lane_id())
; __device__ __forceinline__ void combine_phase(const Ptrs& P, int vcu, int G, int wave, int lane) {
;     ...
;         for (int q = 0; q < 2; ++q) { if (q == 1 && !has1) break;
;             if (pa[q] >= 16384) { const GAS u32x2_t* z0 = (const GAS u32x2_t*)(P.YS + (size_t)MPAD * D + (size_t)pa[q] * D) + lane;
;     ...
;             GAS f32x4* orow = (GAS f32x4*)(P.out + (size_t)mm[q] * D) + lane;
; #pragma unroll
;             for (int j = 0; j < 8; ++j) orow[64 * j] = hv[q][j] + ya[q][j] * ga[q] + yb[q][j] * gb[q]; }
.LBB0_2161:
	v_lshlrev_b32_e32 v114, 16, v80
	v_and_b32_e32 v115, 0xffff0000, v80
	v_lshlrev_b32_e32 v80, 16, v81
	v_and_b32_e32 v81, 0xffff0000, v81
	v_lshlrev_b32_e32 v158, 16, v68
	v_and_b32_e32 v159, 0xffff0000, v68
	v_lshlrev_b32_e32 v160, 16, v69
	v_and_b32_e32 v161, 0xffff0000, v69
	v_lshlrev_b32_e32 v162, 16, v66
	v_and_b32_e32 v163, 0xffff0000, v66
	v_lshlrev_b32_e32 v164, 16, v67
	v_and_b32_e32 v165, 0xffff0000, v67
	v_pk_fma_f32 v[66:67], v[48:49], v[112:113], v[114:115] op_sel_hi:[0,1,1]
	v_pk_fma_f32 v[68:69], v[48:49], v[110:111], v[80:81] op_sel_hi:[0,1,1]
	v_lshlrev_b32_e32 v148, 16, v78
	v_and_b32_e32 v149, 0xffff0000, v78
	v_lshlrev_b32_e32 v78, 16, v79
	v_and_b32_e32 v79, 0xffff0000, v79
	v_pk_fma_f32 v[68:69], v[48:49], v[146:147], v[68:69] op_sel:[1,0,0]
	v_pk_fma_f32 v[66:67], v[48:49], v[144:145], v[66:67] op_sel:[1,0,0]
	global_store_dwordx4 v[10:11], v[66:69], off offset:-4096
	v_lshlrev_b32_e32 v150, 16, v76
	v_and_b32_e32 v151, 0xffff0000, v76
	v_pk_fma_f32 v[66:67], v[48:49], v[108:109], v[148:149] op_sel_hi:[0,1,1]
	v_pk_fma_f32 v[68:69], v[48:49], v[106:107], v[78:79] op_sel_hi:[0,1,1]
	v_lshlrev_b32_e32 v76, 16, v77
	v_and_b32_e32 v77, 0xffff0000, v77
	v_pk_fma_f32 v[68:69], v[48:49], v[142:143], v[68:69] op_sel:[1,0,0]
	v_pk_fma_f32 v[66:67], v[48:49], v[140:141], v[66:67] op_sel:[1,0,0]
	global_store_dwordx4 v[10:11], v[66:69], off offset:-3072
	v_lshlrev_b32_e32 v152, 16, v74
	v_and_b32_e32 v153, 0xffff0000, v74
	v_pk_fma_f32 v[66:67], v[48:49], v[104:105], v[150:151] op_sel_hi:[0,1,1]
	v_pk_fma_f32 v[68:69], v[48:49], v[102:103], v[76:77] op_sel_hi:[0,1,1]
	v_lshlrev_b32_e32 v74, 16, v75
	v_and_b32_e32 v75, 0xffff0000, v75
	v_pk_fma_f32 v[68:69], v[48:49], v[138:139], v[68:69] op_sel:[1,0,0]
	v_pk_fma_f32 v[66:67], v[48:49], v[136:137], v[66:67] op_sel:[1,0,0]
	global_store_dwordx4 v[10:11], v[66:69], off offset:-2048
	v_lshlrev_b32_e32 v154, 16, v72
	v_and_b32_e32 v155, 0xffff0000, v72
	v_pk_fma_f32 v[66:67], v[48:49], v[100:101], v[152:153] op_sel_hi:[0,1,1]
	v_pk_fma_f32 v[68:69], v[48:49], v[98:99], v[74:75] op_sel_hi:[0,1,1]
	v_lshlrev_b32_e32 v72, 16, v73
	v_and_b32_e32 v73, 0xffff0000, v73
	v_pk_fma_f32 v[68:69], v[48:49], v[134:135], v[68:69] op_sel:[1,0,0]
	v_pk_fma_f32 v[66:67], v[48:49], v[132:133], v[66:67] op_sel:[1,0,0]
	global_store_dwordx4 v[10:11], v[66:69], off offset:-1024
	v_lshlrev_b32_e32 v156, 16, v70
	v_and_b32_e32 v157, 0xffff0000, v70
	v_pk_fma_f32 v[66:67], v[48:49], v[96:97], v[154:155] op_sel_hi:[0,1,1]
	v_pk_fma_f32 v[68:69], v[48:49], v[94:95], v[72:73] op_sel_hi:[0,1,1]
	v_lshlrev_b32_e32 v70, 16, v71
	v_and_b32_e32 v71, 0xffff0000, v71
	v_pk_fma_f32 v[68:69], v[48:49], v[130:131], v[68:69] op_sel:[1,0,0]
	v_pk_fma_f32 v[66:67], v[48:49], v[128:129], v[66:67] op_sel:[1,0,0]
	global_store_dwordx4 v[10:11], v[66:69], off
	s_andn2_b64 vcc, exec, s[22:23]
	s_nop 0
	v_pk_fma_f32 v[66:67], v[48:49], v[92:93], v[156:157] op_sel_hi:[0,1,1]
	v_pk_fma_f32 v[68:69], v[48:49], v[90:91], v[70:71] op_sel_hi:[0,1,1]
	v_pk_fma_f32 v[68:69], v[48:49], v[126:127], v[68:69] op_sel:[1,0,0]
	v_pk_fma_f32 v[66:67], v[48:49], v[124:125], v[66:67] op_sel:[1,0,0]
	global_store_dwordx4 v[10:11], v[66:69], off offset:1024
	s_nop 1
	v_pk_fma_f32 v[66:67], v[48:49], v[88:89], v[158:159] op_sel_hi:[0,1,1]
	v_pk_fma_f32 v[68:69], v[48:49], v[86:87], v[160:161] op_sel_hi:[0,1,1]
	v_pk_fma_f32 v[68:69], v[48:49], v[122:123], v[68:69] op_sel:[1,0,0]
	v_pk_fma_f32 v[66:67], v[48:49], v[120:121], v[66:67] op_sel:[1,0,0]
	global_store_dwordx4 v[10:11], v[66:69], off offset:2048
	s_nop 1
	v_pk_fma_f32 v[66:67], v[48:49], v[84:85], v[162:163] op_sel_hi:[0,1,1]
	v_pk_fma_f32 v[68:69], v[48:49], v[82:83], v[164:165] op_sel_hi:[0,1,1]
	v_pk_fma_f32 v[68:69], v[48:49], v[116:117], v[68:69] op_sel:[1,0,0]
	v_pk_fma_f32 v[66:67], v[48:49], v[118:119], v[66:67] op_sel:[1,0,0]
	global_store_dwordx4 v[10:11], v[66:69], off offset:3072
	s_cbranch_vccnz .LBB0_2156
	s_waitcnt vmcnt(23)
	v_lshlrev_b32_e32 v80, 16, v64
	v_and_b32_e32 v81, 0xffff0000, v64
	v_lshlrev_b32_e32 v78, 16, v65
	v_and_b32_e32 v79, 0xffff0000, v65
	s_waitcnt vmcnt(22)
	v_lshlrev_b32_e32 v76, 16, v62
	v_and_b32_e32 v77, 0xffff0000, v62
	v_lshlrev_b32_e32 v74, 16, v63
	v_and_b32_e32 v75, 0xffff0000, v63
	s_waitcnt vmcnt(21)
	v_lshlrev_b32_e32 v72, 16, v60
	v_and_b32_e32 v73, 0xffff0000, v60
	v_lshlrev_b32_e32 v70, 16, v61
	v_and_b32_e32 v71, 0xffff0000, v61
	s_waitcnt vmcnt(20)
	v_lshlrev_b32_e32 v68, 16, v58
	v_and_b32_e32 v69, 0xffff0000, v58
	v_lshlrev_b32_e32 v66, 16, v59
	v_and_b32_e32 v67, 0xffff0000, v59
	s_waitcnt vmcnt(15)
	v_lshlrev_b32_e32 v64, 16, v56
	v_and_b32_e32 v65, 0xffff0000, v56
	v_lshlrev_b32_e32 v62, 16, v57
	v_and_b32_e32 v63, 0xffff0000, v57
	s_waitcnt vmcnt(14)
	v_lshlrev_b32_e32 v60, 16, v54
	v_and_b32_e32 v61, 0xffff0000, v54
	v_lshlrev_b32_e32 v58, 16, v55
	v_and_b32_e32 v59, 0xffff0000, v55
	s_waitcnt vmcnt(13)
	v_lshlrev_b32_e32 v56, 16, v52
	v_and_b32_e32 v57, 0xffff0000, v52
	v_lshlrev_b32_e32 v54, 16, v53
	v_and_b32_e32 v55, 0xffff0000, v53
	s_waitcnt vmcnt(12)
	v_lshlrev_b32_e32 v52, 16, v50
	v_and_b32_e32 v53, 0xffff0000, v50
	v_lshlrev_b32_e32 v48, 16, v51
	s_cmpk_lt_i32 s24, 0x4000
	v_and_b32_e32 v49, 0xffff0000, v51
	s_cbranch_scc1 .LBB0_2164
; #define GAS __attribute__((address_space(1)))
; __device__ __forceinline__ f32x4 bf4_to_f32(u32x2_g a) { return (f32x4){__uint_as_float(a.x << 16), __uint_as_float(a.x & 0xffff0000u), __uint_as_float(a.y << 16), __uint_as_float(a.y & 0xffff0000u)}; }
; #define lane (lane_id())
; __device__ __forceinline__ void combine_phase(const Ptrs& P, int vcu, int G, int wave, int lane) {
;     ...
;             if (pa[q] >= 16384) { const GAS u32x2_t* z0 = (const GAS u32x2_t*)(P.YS + (size_t)MPAD * D + (size_t)pa[q] * D) + lane;
; #pragma unroll
;                 for (int j = 0; j < 8; ++j) ya[q][j] += bf4_to_f32(z0[64 * j]); }
;             if (pb[q] >= 16384) { const GAS u32x2_t* z1 = (const GAS u32x2_t*)(P.YS + (size_t)MPAD * D + (size_t)pb[q] * D) + lane;
; #pragma unroll
;                 for (int j = 0; j < 8; ++j) yb[q][j] += bf4_to_f32(z1[64 * j]); }
	s_mov_b32 s25, s90
	s_lshl_b64 s[22:23], s[24:25], 12
	v_lshl_add_u64 v[50:51], v[6:7], 0, s[22:23]
	global_load_dwordx2 v[166:167], v[50:51], off
	global_load_dwordx2 v[168:169], v[50:51], off offset:512
	global_load_dwordx2 v[170:171], v[50:51], off offset:1024
	global_load_dwordx2 v[172:173], v[50:51], off offset:1536
	global_load_dwordx2 v[174:175], v[50:51], off offset:2048
	global_load_dwordx2 v[176:177], v[50:51], off offset:2560
	global_load_dwordx2 v[178:179], v[50:51], off offset:3072
	global_load_dwordx2 v[180:181], v[50:51], off offset:3584
	s_waitcnt vmcnt(0)
	v_lshlrev_b32_e32 v84, 16, v166
	v_and_b32_e32 v85, 0xffff0000, v166
	v_lshlrev_b32_e32 v82, 16, v167
	v_and_b32_e32 v83, 0xffff0000, v167
	v_pk_add_f32 v[78:79], v[78:79], v[82:83]
	v_pk_add_f32 v[80:81], v[80:81], v[84:85]
	v_lshlrev_b32_e32 v84, 16, v168
	v_and_b32_e32 v85, 0xffff0000, v168
	v_lshlrev_b32_e32 v82, 16, v169
	v_and_b32_e32 v83, 0xffff0000, v169
	v_pk_add_f32 v[74:75], v[74:75], v[82:83]
	v_pk_add_f32 v[76:77], v[76:77], v[84:85]
	v_lshlrev_b32_e32 v84, 16, v170
	v_and_b32_e32 v85, 0xffff0000, v170
	v_lshlrev_b32_e32 v82, 16, v171
	v_and_b32_e32 v83, 0xffff0000, v171
	v_pk_add_f32 v[70:71], v[70:71], v[82:83]
	v_pk_add_f32 v[72:73], v[72:73], v[84:85]
	v_lshlrev_b32_e32 v84, 16, v172
	v_and_b32_e32 v85, 0xffff0000, v172
	v_lshlrev_b32_e32 v82, 16, v173
	v_and_b32_e32 v83, 0xffff0000, v173
	v_pk_add_f32 v[66:67], v[66:67], v[82:83]
	v_pk_add_f32 v[68:69], v[68:69], v[84:85]
	v_lshlrev_b32_e32 v84, 16, v174
	v_and_b32_e32 v85, 0xffff0000, v174
	v_lshlrev_b32_e32 v82, 16, v175
	v_and_b32_e32 v83, 0xffff0000, v175
	v_pk_add_f32 v[62:63], v[62:63], v[82:83]
	v_pk_add_f32 v[64:65], v[64:65], v[84:85]
	v_lshlrev_b32_e32 v84, 16, v176
	v_and_b32_e32 v85, 0xffff0000, v176
	v_lshlrev_b32_e32 v82, 16, v177
	v_and_b32_e32 v83, 0xffff0000, v177
	v_pk_add_f32 v[58:59], v[58:59], v[82:83]
	v_pk_add_f32 v[60:61], v[60:61], v[84:85]
	v_lshlrev_b32_e32 v84, 16, v178
	v_and_b32_e32 v85, 0xffff0000, v178
	v_lshlrev_b32_e32 v82, 16, v179
	v_and_b32_e32 v83, 0xffff0000, v179
	v_pk_add_f32 v[54:55], v[54:55], v[82:83]
	v_lshlrev_b32_e32 v82, 16, v180
	v_and_b32_e32 v83, 0xffff0000, v180
	v_lshlrev_b32_e32 v50, 16, v181
	v_and_b32_e32 v51, 0xffff0000, v181
	v_pk_add_f32 v[56:57], v[56:57], v[84:85]
	v_pk_add_f32 v[48:49], v[48:49], v[50:51]
	v_pk_add_f32 v[52:53], v[52:53], v[82:83]
.LBB0_2164:
	v_lshlrev_b32_e32 v92, 16, v46
	v_and_b32_e32 v93, 0xffff0000, v46
	v_lshlrev_b32_e32 v94, 16, v47
	v_and_b32_e32 v95, 0xffff0000, v47
	v_lshlrev_b32_e32 v88, 16, v44
	v_and_b32_e32 v89, 0xffff0000, v44
	v_lshlrev_b32_e32 v90, 16, v45
	v_and_b32_e32 v91, 0xffff0000, v45
	v_lshlrev_b32_e32 v84, 16, v42
	v_and_b32_e32 v85, 0xffff0000, v42
	v_lshlrev_b32_e32 v86, 16, v43
	v_and_b32_e32 v87, 0xffff0000, v43
	v_lshlrev_b32_e32 v50, 16, v38
	v_and_b32_e32 v51, 0xffff0000, v38
	v_lshlrev_b32_e32 v82, 16, v39
	v_and_b32_e32 v83, 0xffff0000, v39
	s_waitcnt vmcnt(11)
	v_lshlrev_b32_e32 v44, 16, v40
	v_and_b32_e32 v45, 0xffff0000, v40
	v_lshlrev_b32_e32 v46, 16, v41
	v_and_b32_e32 v47, 0xffff0000, v41
	s_waitcnt vmcnt(10)
	v_lshlrev_b32_e32 v40, 16, v36
	v_and_b32_e32 v41, 0xffff0000, v36
	v_lshlrev_b32_e32 v42, 16, v37
	v_and_b32_e32 v43, 0xffff0000, v37
	s_waitcnt vmcnt(9)
	v_lshlrev_b32_e32 v36, 16, v34
	v_and_b32_e32 v37, 0xffff0000, v34
	v_lshlrev_b32_e32 v38, 16, v35
	v_and_b32_e32 v39, 0xffff0000, v35
	s_waitcnt vmcnt(8)
	v_lshlrev_b32_e32 v34, 16, v32
	v_and_b32_e32 v35, 0xffff0000, v32
	v_lshlrev_b32_e32 v32, 16, v33
	s_cmpk_lt_i32 s20, 0x4000
	v_and_b32_e32 v33, 0xffff0000, v33
	s_cbranch_scc1 .LBB0_2155
	s_mov_b32 s21, s90
	s_lshl_b64 s[20:21], s[20:21], 12
	v_lshl_add_u64 v[96:97], v[6:7], 0, s[20:21]
	global_load_dwordx2 v[166:167], v[96:97], off
	global_load_dwordx2 v[168:169], v[96:97], off offset:512
	global_load_dwordx2 v[170:171], v[96:97], off offset:1024
	global_load_dwordx2 v[172:173], v[96:97], off offset:1536
	global_load_dwordx2 v[174:175], v[96:97], off offset:2048
	global_load_dwordx2 v[176:177], v[96:97], off offset:2560
	global_load_dwordx2 v[178:179], v[96:97], off offset:3072
	global_load_dwordx2 v[180:181], v[96:97], off offset:3584
	s_waitcnt vmcnt(0)
	v_lshlrev_b32_e32 v100, 16, v166
	v_and_b32_e32 v101, 0xffff0000, v166
	v_lshlrev_b32_e32 v98, 16, v167
	v_and_b32_e32 v99, 0xffff0000, v167
	v_pk_add_f32 v[94:95], v[94:95], v[98:99]
	v_pk_add_f32 v[92:93], v[92:93], v[100:101]
	v_lshlrev_b32_e32 v100, 16, v168
	v_and_b32_e32 v101, 0xffff0000, v168
	v_lshlrev_b32_e32 v98, 16, v169
	v_and_b32_e32 v99, 0xffff0000, v169
	v_pk_add_f32 v[90:91], v[90:91], v[98:99]
	v_pk_add_f32 v[88:89], v[88:89], v[100:101]
	v_lshlrev_b32_e32 v100, 16, v170
	v_and_b32_e32 v101, 0xffff0000, v170
	v_lshlrev_b32_e32 v98, 16, v171
	v_and_b32_e32 v99, 0xffff0000, v171
	v_pk_add_f32 v[86:87], v[86:87], v[98:99]
	v_pk_add_f32 v[84:85], v[84:85], v[100:101]
	v_lshlrev_b32_e32 v100, 16, v172
	v_and_b32_e32 v101, 0xffff0000, v172
	v_lshlrev_b32_e32 v98, 16, v173
	v_and_b32_e32 v99, 0xffff0000, v173
	v_pk_add_f32 v[82:83], v[82:83], v[98:99]
	v_pk_add_f32 v[50:51], v[50:51], v[100:101]
	v_lshlrev_b32_e32 v100, 16, v174
	v_and_b32_e32 v101, 0xffff0000, v174
	v_lshlrev_b32_e32 v98, 16, v175
	v_and_b32_e32 v99, 0xffff0000, v175
	v_pk_add_f32 v[46:47], v[46:47], v[98:99]
	v_pk_add_f32 v[44:45], v[44:45], v[100:101]
	v_lshlrev_b32_e32 v100, 16, v176
	v_and_b32_e32 v101, 0xffff0000, v176
	v_lshlrev_b32_e32 v98, 16, v177
	v_and_b32_e32 v99, 0xffff0000, v177
	v_pk_add_f32 v[42:43], v[42:43], v[98:99]
	v_pk_add_f32 v[40:41], v[40:41], v[100:101]
	v_lshlrev_b32_e32 v100, 16, v178
	v_and_b32_e32 v101, 0xffff0000, v178
	v_lshlrev_b32_e32 v98, 16, v179
	v_and_b32_e32 v99, 0xffff0000, v179
	v_pk_add_f32 v[38:39], v[38:39], v[98:99]
	v_lshlrev_b32_e32 v98, 16, v180
	v_and_b32_e32 v99, 0xffff0000, v180
	v_lshlrev_b32_e32 v96, 16, v181
	v_and_b32_e32 v97, 0xffff0000, v181
	v_pk_add_f32 v[36:37], v[36:37], v[100:101]
	v_pk_add_f32 v[32:33], v[32:33], v[96:97]
	v_pk_add_f32 v[34:35], v[34:35], v[98:99]
	s_branch .LBB0_2155

; __device__ __forceinline__ unsigned xb_ld(unsigned* p)              { return __hip_atomic_load(p, __ATOMIC_RELAXED, __HIP_MEMORY_SCOPE_AGENT); }
; __device__ __forceinline__ unsigned xb_add(unsigned* p, unsigned v) { return __hip_atomic_fetch_add(p, v, __ATOMIC_RELAXED, __HIP_MEMORY_SCOPE_AGENT); }
; #define XB_SPIN(cond, bar) do { unsigned _sp = 0; while (cond) { __builtin_amdgcn_s_sleep(1); \
;     if ((++_sp & 255u) == 0u) { if (xb_ld(&(bar)[XB_TMO])) break; if (_sp > XB_SPIN_CAP) { atomicAdd(&(bar)[XB_TMO], 1u); break; } } } } while (0)
; __device__ __forceinline__ void xcd_barrier(const XcdBarrier& b) {
;     ...
;         unsigned nloc = b.st[0], nx = b.st[1];
;         if (nloc == 0u) { xcd_barrier_complete(bar, b.x, nloc, nx); b.st[0] = nloc; b.st[1] = nx; }
;         const unsigned old = xb_add(&bar[XB_XSUB(b.x)], 1u);
;         const unsigned gen = old / nloc;
;         if (old + 1u == (gen + 1u) * nloc) {
;             __builtin_amdgcn_fence(__ATOMIC_RELEASE, "agent");
;             asm volatile("s_waitcnt vmcnt(0)" ::: "memory");
;             const unsigned og = xb_add(&bar[XB_TOP], 1u);
;             const unsigned tg = og / nx;
;             if (og + 1u == (tg + 1u) * nx) xb_add(&bar[XB_TOPGEN], 1u);
;             else XB_SPIN(xb_ld(&bar[XB_TOPGEN]) == tg, bar);
;             __builtin_amdgcn_fence(__ATOMIC_ACQUIRE, "agent");
;             xb_add(&bar[XB_XGEN(b.x)], 1u);
;             asm volatile("s_waitcnt vmcnt(0)" ::: "memory");
;         } else {
;             XB_SPIN(xb_ld(&bar[XB_XGEN(b.x)]) == gen, bar);
.LBB0_2188:
	s_or_b64 exec, exec, s[20:21]
	v_cvt_f32_u32_e32 v5, v3
	s_waitcnt vmcnt(0)
	v_readfirstlane_b32 s18, v4
	v_sub_u32_e32 v4, 0, v3
	v_rcp_iflag_f32_e32 v5, v5
	v_add_u32_e32 v6, s18, v0
	v_mul_f32_e32 v5, 0x4f7ffffe, v5
	v_cvt_u32_f32_e32 v5, v5
	v_mul_lo_u32 v0, v4, v5
	v_mul_hi_u32 v0, v5, v0
	v_add_u32_e32 v0, v5, v0
	v_mul_hi_u32 v0, v6, v0
	v_mul_lo_u32 v4, v0, v3
	v_sub_u32_e32 v4, v6, v4
	v_add_u32_e32 v5, 1, v0
	v_cmp_ge_u32_e32 vcc, v4, v3
	s_nop 1
	v_cndmask_b32_e32 v0, v0, v5, vcc
	v_sub_u32_e32 v5, v4, v3
	v_cndmask_b32_e32 v4, v4, v5, vcc
	v_add_u32_e32 v5, 1, v0
	v_cmp_ge_u32_e32 vcc, v4, v3
	v_add_u32_e32 v4, 1, v6
	s_nop 0
	v_cndmask_b32_e32 v0, v0, v5, vcc
	v_mul_lo_u32 v5, v3, v0
	v_add_u32_e32 v3, v5, v3
	v_cmp_ne_u32_e32 vcc, v4, v3
	s_and_saveexec_b64 s[18:19], vcc
	s_xor_b64 s[20:21], exec, s[18:19]
	s_cbranch_execz .LBB0_2202
	s_waitcnt lgkmcnt(0)
	buffer_inv sc1
	v_mov_b32_e32 v2, 0x2000
	global_load_dword v2, v2, s[16:17] offset:1024 sc1
	s_add_u32 s18, s16, 0x2400
	s_addc_u32 s19, s17, 0
	s_waitcnt vmcnt(0)
	v_cmp_eq_u32_e32 vcc, v2, v0
	s_and_saveexec_b64 s[22:23], vcc
	s_cbranch_execz .LBB0_2201
	s_mov_b32 s36, 1
	s_mov_b64 s[24:25], 0
	s_branch .LBB0_2192

; __device__ __forceinline__ unsigned xb_ld(unsigned* p)              { return __hip_atomic_load(p, __ATOMIC_RELAXED, __HIP_MEMORY_SCOPE_AGENT); }
; __device__ __forceinline__ unsigned xb_add(unsigned* p, unsigned v) { return __hip_atomic_fetch_add(p, v, __ATOMIC_RELAXED, __HIP_MEMORY_SCOPE_AGENT); }
; #define XB_SPIN(cond, bar) do { unsigned _sp = 0; while (cond) { __builtin_amdgcn_s_sleep(1); \
;     if ((++_sp & 255u) == 0u) { if (xb_ld(&(bar)[XB_TMO])) break; if (_sp > XB_SPIN_CAP) { atomicAdd(&(bar)[XB_TMO], 1u); break; } } } } while (0)
; __device__ __forceinline__ void xcd_barrier(const XcdBarrier& b) {
;     ...
;         if (old + 1u == (gen + 1u) * nloc) {
;             __builtin_amdgcn_fence(__ATOMIC_RELEASE, "agent");
;             asm volatile("s_waitcnt vmcnt(0)" ::: "memory");
;             const unsigned og = xb_add(&bar[XB_TOP], 1u);
;             const unsigned tg = og / nx;
;             if (og + 1u == (tg + 1u) * nx) xb_add(&bar[XB_TOPGEN], 1u);
;             else XB_SPIN(xb_ld(&bar[XB_TOPGEN]) == tg, bar);
;             __builtin_amdgcn_fence(__ATOMIC_ACQUIRE, "agent");
;             xb_add(&bar[XB_XGEN(b.x)], 1u);
.LBB0_2203:
	s_mov_b64 s[18:19], exec
	buffer_wbl2 sc1
	s_waitcnt lgkmcnt(0)
	s_waitcnt vmcnt(0)
	buffer_inv sc1
	v_mbcnt_lo_u32_b32 v0, s18, 0
	v_mbcnt_hi_u32_b32 v0, s19, v0
	v_cmp_eq_u32_e32 vcc, 0, v0
	s_and_saveexec_b64 s[20:21], vcc
	s_cbranch_execz .LBB0_2205
	s_bcnt1_i32_b64 s18, s[18:19]
	v_mov_b32_e32 v3, s18
	v_mov_b32_e32 v4, 0x3000
	global_atomic_add v3, v4, v3, s[14:15] offset:1024 sc0

; __device__ __forceinline__ unsigned xb_ld(unsigned* p)              { return __hip_atomic_load(p, __ATOMIC_RELAXED, __HIP_MEMORY_SCOPE_AGENT); }
; __device__ __forceinline__ unsigned xb_add(unsigned* p, unsigned v) { return __hip_atomic_fetch_add(p, v, __ATOMIC_RELAXED, __HIP_MEMORY_SCOPE_AGENT); }
; #define XB_SPIN(cond, bar) do { unsigned _sp = 0; while (cond) { __builtin_amdgcn_s_sleep(1); \
;     if ((++_sp & 255u) == 0u) { if (xb_ld(&(bar)[XB_TMO])) break; if (_sp > XB_SPIN_CAP) { atomicAdd(&(bar)[XB_TMO], 1u); break; } } } } while (0)
; __device__ __forceinline__ void xcd_barrier(const XcdBarrier& b) {
;     ...
;             const unsigned og = xb_add(&bar[XB_TOP], 1u);
;             const unsigned tg = og / nx;
;             if (og + 1u == (tg + 1u) * nx) xb_add(&bar[XB_TOPGEN], 1u);
;             else XB_SPIN(xb_ld(&bar[XB_TOPGEN]) == tg, bar);
;             __builtin_amdgcn_fence(__ATOMIC_ACQUIRE, "agent");
;             xb_add(&bar[XB_XGEN(b.x)], 1u);
.LBB0_2219:
	s_or_b64 exec, exec, s[14:15]
	s_mov_b64 s[14:15], exec
	v_mbcnt_lo_u32_b32 v0, s14, 0
	v_mbcnt_hi_u32_b32 v0, s15, v0
	v_cmp_eq_u32_e32 vcc, 0, v0
	s_waitcnt vmcnt(0)
	s_and_saveexec_b64 s[18:19], vcc
	s_cbranch_execnz .LBB0_2220
	s_getpc_b64 s[98:99]
